# v31 plus leaner LDS-DMA issue groups in converter and KV loader blocks
# baseline (speedup 1.0000x reference)
.LBB0_541:
	s_add_i32 s33, s15, 0xffff0000
	s_cmp_lt_i32 s15, 0x10000
	s_cselect_b32 s33, s15, s33
	s_cselect_b32 s41, s30, 0x1ff
	s_cselect_b32 s42, 10, 11
	s_cselect_b32 s40, 10, 9
	s_cselect_b32 s43, s11, s13
	s_cselect_b32 s44, s10, s12
	s_cselect_b32 s45, 21, 20
	s_and_b32 s41, s33, s41
	s_add_i32 s56, s42, -5
	s_lshr_b32 s41, s41, s56
	s_ashr_i32 s40, s33, s40
	s_lshl_b32 s57, s41, 6
	s_lshl_b32 s41, -1, s56
	s_andn2_b32 s33, s33, s41
	s_ashr_i32 s41, s40, 31
	s_lshl_b64 s[40:41], s[40:41], s45
	s_lshl_b64 s[40:41], s[40:41], 2
	s_add_u32 s40, s44, s40
	s_addc_u32 s41, s43, s41
	s_lshl_b32 s43, s57, s42
	v_mov_b32_e32 v2, v0
	s_lshl_b32 s43, s43, 2
	s_add_u32 s40, s40, s43
	v_bfe_u32 v68, v2, 3, 3
	v_lshlrev_b32_e32 v68, s42, v68
	s_addc_u32 s41, s41, 0
	s_lshl_b32 s33, s33, 7
	v_lshlrev_b32_e32 v2, 4, v2
	v_lshlrev_b32_e32 v68, 2, v68
	s_add_u32 s40, s40, s33
	v_and_b32_e32 v69, 0x70, v2
	s_addc_u32 s41, s41, 0
	v_or_b32_e32 v70, v68, v69
	s_mov_b32 m0, s23
	s_nop 0
	global_load_lds_dwordx4 v70, s[40:41] nt
	s_lshl_b32 s33, 32, s42
	s_add_u32 s56, s40, s33
	s_addc_u32 s57, s41, 0
	v_bitop3_b32 v70, v68, 16, v69 bitop3:0x36
	s_mov_b32 m0, s86
	s_nop 0
	global_load_lds_dwordx4 v70, s[56:57] nt
	s_lshl_b32 s33, 64, s42
	s_add_u32 s56, s40, s33
	s_addc_u32 s57, s41, 0
	v_bitop3_b32 v70, v68, 32, v69 bitop3:0x36
	s_mov_b32 m0, s87
	s_nop 0
	global_load_lds_dwordx4 v70, s[56:57] nt
	s_lshl_b32 s33, 0x60, s42
	s_add_u32 s56, s40, s33
	s_addc_u32 s57, s41, 0
	v_bitop3_b32 v70, v68, 48, v69 bitop3:0x36
	s_mov_b32 m0, s88
	s_nop 0
	global_load_lds_dwordx4 v70, s[56:57] nt
	s_lshl_b32 s33, 0x80, s42
	s_add_u32 s56, s40, s33
	s_addc_u32 s57, s41, 0
	v_bitop3_b32 v70, v68, 64, v69 bitop3:0x36
	s_mov_b32 m0, s89
	s_nop 0
	global_load_lds_dwordx4 v70, s[56:57] nt
	s_lshl_b32 s33, 0xa0, s42
	s_add_u32 s56, s40, s33
	s_addc_u32 s57, s41, 0
	v_bitop3_b32 v70, v68, s31, v69 bitop3:0x36
	s_mov_b32 m0, s90
	s_nop 0
	global_load_lds_dwordx4 v70, s[56:57] nt
	s_lshl_b32 s33, 0xc0, s42
	s_add_u32 s56, s40, s33
	s_addc_u32 s57, s41, 0
	v_bitop3_b32 v69, v68, s61, v69 bitop3:0x36
	s_mov_b32 m0, s91
	s_nop 0
	global_load_lds_dwordx4 v69, s[56:57] nt
	s_lshl_b32 s33, 0xe0, s42
	s_add_u32 s40, s40, s33
	s_addc_u32 s41, s41, 0
	v_bitop3_b32 v2, v68, s62, v2 bitop3:0x34
	s_mov_b32 m0, s92
	s_nop 0
	global_load_lds_dwordx4 v2, s[40:41] nt
	s_add_i32 s59, s15, s22
	s_mov_b32 s33, s15
	s_sub_i32 s15, s63, 63
	s_cmp_gt_i32 s15, s16
	s_cbranch_scc0 .LBB0_552

.LBB0_549:
	s_add_i32 s6, s59, 0xffff0000
	s_cmp_lt_i32 s59, 0x10000
	s_cselect_b32 s7, s59, s6
	s_cselect_b32 s15, s30, 0x1ff
	s_cselect_b32 s33, 10, 11
	s_cselect_b32 s6, 10, 9
	s_cselect_b32 s40, s11, s13
	s_cselect_b32 s41, s10, s12
	s_cselect_b32 s42, 21, 20
	s_and_b32 s15, s7, s15
	s_add_i32 s43, s33, -5
	s_ashr_i32 s6, s7, s6
	s_lshr_b32 s15, s15, s43
	s_lshl_b32 s43, -1, s43
	s_andn2_b32 s43, s7, s43
	s_ashr_i32 s7, s6, 31
	s_lshl_b64 s[6:7], s[6:7], s42
	s_lshl_b32 s15, s15, 6
	s_lshl_b64 s[6:7], s[6:7], 2
	s_add_u32 s6, s41, s6
	s_addc_u32 s7, s40, s7
	s_lshl_b32 s15, s15, s33
	v_mov_b32_e32 v2, v0
	s_lshl_b32 s15, s15, 2
	s_add_u32 s6, s6, s15
	v_bfe_u32 v68, v2, 3, 3
	v_lshlrev_b32_e32 v68, s33, v68
	s_addc_u32 s7, s7, 0
	s_lshl_b32 s15, s43, 7
	v_lshlrev_b32_e32 v2, 4, v2
	v_lshlrev_b32_e32 v68, 2, v68
	s_add_u32 s6, s6, s15
	v_and_b32_e32 v69, 0x70, v2
	s_addc_u32 s7, s7, 0
	v_or_b32_e32 v70, v68, v69
	s_mov_b32 m0, s71
	s_nop 0
	global_load_lds_dwordx4 v70, s[6:7] nt
	s_lshl_b32 s15, 32, s33
	s_add_u32 s40, s6, s15
	s_addc_u32 s41, s7, 0
	v_bitop3_b32 v70, v68, 16, v69 bitop3:0x36
	s_mov_b32 m0, s93
	s_nop 0
	global_load_lds_dwordx4 v70, s[40:41] nt
	s_lshl_b32 s15, 64, s33
	s_add_u32 s40, s6, s15
	s_addc_u32 s41, s7, 0
	v_bitop3_b32 v70, v68, 32, v69 bitop3:0x36
	s_mov_b32 m0, s94
	s_nop 0
	global_load_lds_dwordx4 v70, s[40:41] nt
	s_lshl_b32 s15, 0x60, s33
	s_add_u32 s40, s6, s15
	s_addc_u32 s41, s7, 0
	v_bitop3_b32 v70, v68, 48, v69 bitop3:0x36
	s_mov_b32 m0, s95
	s_nop 0
	global_load_lds_dwordx4 v70, s[40:41] nt
	s_lshl_b32 s15, 0x80, s33
	s_add_u32 s40, s6, s15
	s_addc_u32 s41, s7, 0
	v_bitop3_b32 v70, v68, 64, v69 bitop3:0x36
	s_mov_b32 m0, s96
	s_nop 0
	global_load_lds_dwordx4 v70, s[40:41] nt
	s_lshl_b32 s15, 0xa0, s33
	s_add_u32 s40, s6, s15
	s_addc_u32 s41, s7, 0
	v_bitop3_b32 v70, v68, s31, v69 bitop3:0x36
	s_mov_b32 m0, s97
	s_nop 0
	global_load_lds_dwordx4 v70, s[40:41] nt
	s_lshl_b32 s15, 0xc0, s33
	s_add_u32 s40, s6, s15
	s_addc_u32 s41, s7, 0
	v_bitop3_b32 v69, v68, s61, v69 bitop3:0x36
	s_mov_b32 m0, s27
	s_nop 0
	global_load_lds_dwordx4 v69, s[40:41] nt
	s_lshl_b32 s15, 0xe0, s33
	s_add_u32 s6, s6, s15
	s_addc_u32 s7, s7, 0
	v_bitop3_b32 v2, v68, s62, v2 bitop3:0x34
	s_mov_b32 m0, s26
	s_nop 0
	global_load_lds_dwordx4 v2, s[6:7] nt
	s_add_i32 s15, s59, s22
	s_mov_b32 s33, s59
	s_add_i32 s6, s63, 1
	s_cmp_gt_i32 s6, s16
	s_cbranch_scc1 .LBB0_532
	s_branch .LBB0_567

.LBB0_1430:
	s_or_b32 s8, s19, 1
	s_cmp_ge_u32 s8, s41
	s_waitcnt lgkmcnt(0)
	s_barrier
	s_cselect_b64 s[8:9], -1, 0
	s_xor_b64 s[58:59], s[20:21], -1
	s_or_b64 s[8:9], s[58:59], s[8:9]
	s_and_b64 vcc, exec, s[8:9]
	s_cbranch_vccnz .LBB0_1433
	s_add_u32 s8, s54, 0xfff00000
	s_addc_u32 s9, s55, -1
	s_mov_b32 m0, s79
	s_nop 0
	global_load_lds_dwordx4 v1, s[8:9]
	s_mov_b32 m0, s89
	s_nop 0
	global_load_lds_dwordx4 v178, s[8:9]
	s_mov_b32 m0, s90
	s_nop 0
	global_load_lds_dwordx4 v179, s[8:9]
	s_mov_b32 m0, s91
	s_nop 0
	global_load_lds_dwordx4 v180, s[8:9]
	s_add_u32 s8, s56, 0xfff00000
	s_addc_u32 s9, s57, -1
	s_mov_b32 m0, s80
	s_nop 0
	global_load_lds_dwordx4 v133, s[8:9]
	s_and_b64 vcc, exec, s[6:7]
	s_mov_b32 m0, s92
	s_nop 0
	global_load_lds_dwordx4 v181, s[8:9]
	s_mov_b32 m0, s93
	s_nop 0
	global_load_lds_dwordx4 v182, s[8:9]
	s_mov_b32 m0, s94
	s_nop 0
	global_load_lds_dwordx4 v183, s[8:9]
	s_cbranch_vccnz .LBB0_1433
	s_add_u32 s8, s52, 0xffffff00
	s_addc_u32 s9, s53, -1
	s_mov_b32 s42, m0
	s_mov_b32 m0, s83
	s_nop 0
	global_load_lds_dword v175, s[8:9]
	s_mov_b32 m0, s42

.LBB0_1436:
	s_add_i32 s42, s73, 0xffff0000
	s_cmp_lt_i32 s73, 0x10000
	s_cselect_b32 s43, s73, s42
	s_cselect_b32 s44, s1, 0x1ff
	s_cselect_b32 s45, 10, 11
	s_cselect_b32 s42, 10, 9
	s_cselect_b32 s46, s13, s15
	s_cselect_b32 s47, s12, s14
	s_cselect_b32 s58, 21, 20
	s_and_b32 s44, s43, s44
	s_add_i32 s59, s45, -5
	s_ashr_i32 s42, s43, s42
	s_lshr_b32 s44, s44, s59
	s_lshl_b32 s59, -1, s59
	s_andn2_b32 s59, s43, s59
	s_ashr_i32 s43, s42, 31
	s_lshl_b64 s[42:43], s[42:43], s58
	s_lshl_b32 s44, s44, 6
	s_lshl_b64 s[42:43], s[42:43], 2
	s_add_u32 s42, s47, s42
	s_addc_u32 s43, s46, s43
	s_lshl_b32 s44, s44, s45
	v_mov_b32_e32 v2, v0
	s_lshl_b32 s44, s44, 2
	s_add_u32 s42, s42, s44
	v_bfe_u32 v68, v2, 3, 3
	v_lshlrev_b32_e32 v68, s45, v68
	s_addc_u32 s43, s43, 0
	s_lshl_b32 s44, s59, 7
	v_lshlrev_b32_e32 v2, 4, v2
	v_lshlrev_b32_e32 v68, 2, v68
	s_add_u32 s42, s42, s44
	v_and_b32_e32 v69, 0x70, v2
	s_addc_u32 s43, s43, 0
	v_or_b32_e32 v70, v68, v69
	s_mov_b32 m0, s65
	s_nop 0
	global_load_lds_dwordx4 v70, s[42:43] nt
	s_lshl_b32 s44, 32, s45
	s_add_u32 s58, s42, s44
	s_addc_u32 s59, s43, 0
	v_bitop3_b32 v70, v68, 16, v69 bitop3:0x36
	s_mov_b32 m0, s95
	s_nop 0
	global_load_lds_dwordx4 v70, s[58:59] nt
	s_lshl_b32 s44, 64, s45
	s_add_u32 s58, s42, s44
	s_addc_u32 s59, s43, 0
	v_bitop3_b32 v70, v68, 32, v69 bitop3:0x36
	s_mov_b32 m0, s96
	s_nop 0
	global_load_lds_dwordx4 v70, s[58:59] nt
	s_lshl_b32 s44, 0x60, s45
	s_add_u32 s58, s42, s44
	s_addc_u32 s59, s43, 0
	v_bitop3_b32 v70, v68, 48, v69 bitop3:0x36
	s_mov_b32 m0, s97
	s_nop 0
	global_load_lds_dwordx4 v70, s[58:59] nt
	s_lshl_b32 s44, 0x80, s45
	s_add_u32 s58, s42, s44
	s_addc_u32 s59, s43, 0
	v_bitop3_b32 v70, v68, 64, v69 bitop3:0x36
	s_mov_b32 m0, s30
	s_nop 0
	global_load_lds_dwordx4 v70, s[58:59] nt
	s_lshl_b32 s44, 0xa0, s45
	s_add_u32 s58, s42, s44
	s_addc_u32 s59, s43, 0
	v_bitop3_b32 v70, v68, s26, v69 bitop3:0x36
	s_mov_b32 m0, s31
	s_nop 0
	global_load_lds_dwordx4 v70, s[58:59] nt
	s_lshl_b32 s44, 0xc0, s45
	s_add_u32 s58, s42, s44
	s_addc_u32 s59, s43, 0
	v_bitop3_b32 v69, v68, s74, v69 bitop3:0x36
	s_mov_b32 m0, s22
	s_nop 0
	global_load_lds_dwordx4 v69, s[58:59] nt
	s_lshl_b32 s44, 0xe0, s45
	s_add_u32 s42, s42, s44
	s_addc_u32 s43, s43, 0
	v_bitop3_b32 v2, v68, s0, v2 bitop3:0x34
	s_mov_b32 m0, s23
	s_nop 0
	global_load_lds_dwordx4 v2, s[42:43] nt
	s_add_i32 s72, s73, s64
	s_mov_b32 s70, s73
	s_sub_i32 s42, s18, 63
	s_cmp_gt_i32 s42, s75
	s_cbranch_scc0 .LBB0_1448

.LBB0_1445:
	s_add_i32 s8, s72, 0xffff0000
	s_cmp_lt_i32 s72, 0x10000
	s_cselect_b32 s9, s72, s8
	s_cselect_b32 s42, s1, 0x1ff
	s_cselect_b32 s44, 10, 11
	s_cselect_b32 s8, 10, 9
	s_cselect_b32 s43, s13, s15
	s_cselect_b32 s45, s12, s14
	s_cselect_b32 s46, 21, 20
	s_and_b32 s42, s9, s42
	s_add_i32 s47, s44, -5
	s_ashr_i32 s8, s9, s8
	s_lshr_b32 s42, s42, s47
	s_lshl_b32 s47, -1, s47
	s_andn2_b32 s47, s9, s47
	s_ashr_i32 s9, s8, 31
	s_lshl_b64 s[8:9], s[8:9], s46
	s_lshl_b32 s42, s42, 6
	s_lshl_b64 s[8:9], s[8:9], 2
	s_add_u32 s8, s45, s8
	s_addc_u32 s9, s43, s9
	s_lshl_b32 s42, s42, s44
	v_mov_b32_e32 v2, v0
	s_lshl_b32 s42, s42, 2
	s_add_u32 s8, s8, s42
	v_bfe_u32 v68, v2, 3, 3
	v_lshlrev_b32_e32 v68, s44, v68
	s_addc_u32 s9, s9, 0
	s_lshl_b32 s42, s47, 7
	v_lshlrev_b32_e32 v2, 4, v2
	v_lshlrev_b32_e32 v68, 2, v68
	s_add_u32 s8, s8, s42
	v_and_b32_e32 v69, 0x70, v2
	s_addc_u32 s9, s9, 0
	v_or_b32_e32 v70, v68, v69
	s_mov_b32 m0, s82
	s_nop 0
	global_load_lds_dwordx4 v70, s[8:9] nt
	s_lshl_b32 s42, 32, s44
	s_add_u32 s42, s8, s42
	s_addc_u32 s43, s9, 0
	v_bitop3_b32 v70, v68, 16, v69 bitop3:0x36
	s_mov_b32 m0, s28
	s_nop 0
	global_load_lds_dwordx4 v70, s[42:43] nt
	s_lshl_b32 s42, 64, s44
	s_add_u32 s42, s8, s42
	s_addc_u32 s43, s9, 0
	v_bitop3_b32 v70, v68, 32, v69 bitop3:0x36
	s_mov_b32 m0, s29
	s_nop 0
	global_load_lds_dwordx4 v70, s[42:43] nt
	s_lshl_b32 s42, 0x60, s44
	s_add_u32 s42, s8, s42
	s_addc_u32 s43, s9, 0
	v_bitop3_b32 v70, v68, 48, v69 bitop3:0x36
	s_mov_b32 m0, s33
	s_nop 0
	global_load_lds_dwordx4 v70, s[42:43] nt
	s_lshl_b32 s42, 0x80, s44
	s_add_u32 s42, s8, s42
	s_addc_u32 s43, s9, 0
	v_bitop3_b32 v70, v68, 64, v69 bitop3:0x36
	s_mov_b32 m0, s3
	s_nop 0
	global_load_lds_dwordx4 v70, s[42:43] nt
	s_lshl_b32 s42, 0xa0, s44
	s_add_u32 s42, s8, s42
	s_addc_u32 s43, s9, 0
	v_bitop3_b32 v70, v68, s26, v69 bitop3:0x36
	s_mov_b32 m0, s2
	s_nop 0
	global_load_lds_dwordx4 v70, s[42:43] nt
	s_lshl_b32 s42, 0xc0, s44
	s_add_u32 s42, s8, s42
	s_addc_u32 s43, s9, 0
	v_bitop3_b32 v69, v68, s74, v69 bitop3:0x36
	s_mov_b32 m0, s67
	s_nop 0
	global_load_lds_dwordx4 v69, s[42:43] nt
	s_lshl_b32 s42, 0xe0, s44
	s_add_u32 s8, s8, s42
	s_addc_u32 s9, s9, 0
	v_bitop3_b32 v2, v68, s0, v2 bitop3:0x34
	s_mov_b32 m0, s66
	s_nop 0
	global_load_lds_dwordx4 v2, s[8:9] nt
	s_add_i32 s73, s72, s64
	s_mov_b32 s70, s72
	s_add_i32 s8, s18, 1
	s_cmp_gt_i32 s8, s75
	s_cbranch_scc1 .LBB0_1426
	s_branch .LBB0_1463
